# speedup vs baseline: 1.0546x; 1.0133x over previous
_Z8k3_chainPKfPK15HIP_vector_typeIiLj4EEPKtS6_S0_S0_Pf:
	s_load_dwordx8 s[8:15], s[0:1], 0x0
	s_load_dwordx4 s[4:7], s[0:1], 0x20
	s_load_dwordx2 s[16:17], s[0:1], 0x30
	s_mul_hi_u32 s0, s2, 0xaaaaaaab
	s_lshr_b32 s20, s0, 5
	s_mul_i32 s0, s20, 48
	s_mov_b32 s21, 0
	s_sub_i32 s18, s2, s0
	s_lshl_b64 s[0:1], s[20:21], 13
	s_waitcnt lgkmcnt(0)
	s_add_u32 s2, s10, s0
	v_and_b32_e32 v1, 3, v0
	s_addc_u32 s3, s11, s1
	s_mul_hi_u32 s1, s20, 0x18000
	s_mul_i32 s0, s20, 0x18000
	v_lshlrev_b32_e32 v104, 4, v0
	v_mov_b32_e32 v105, 0
	v_lshl_or_b32 v98, s18, 2, v1
	s_lshl_b64 s[18:19], s[0:1], 4
	v_lshl_add_u64 v[2:3], s[2:3], 0, v[104:105]
	s_add_u32 s0, s8, s18
	s_movk_i32 s8, 0x1000
	v_add_co_u32_e32 v10, vcc, s8, v2
	s_addc_u32 s1, s9, s19
	s_nop 0
	v_addc_co_u32_e32 v11, vcc, 0, v3, vcc
	global_load_dwordx4 v[2:5], v104, s[2:3]
	global_load_dwordx4 v[6:9], v[10:11], off
	s_mul_i32 s2, s20, 0x6000
	s_mul_hi_u32 s3, s20, 0x6000
	s_add_u32 s2, s12, s2
	s_addc_u32 s3, s13, s3
	v_lshl_add_u64 v[10:11], s[2:3], 0, v[104:105]
	s_movk_i32 s8, 0x2000
	v_add_co_u32_e32 v12, vcc, s8, v10
	s_movk_i32 s8, 0x3000
	s_nop 0
	v_addc_co_u32_e32 v13, vcc, 0, v11, vcc
	global_load_dwordx4 v[38:41], v104, s[2:3]
	global_load_dwordx4 v[42:45], v[12:13], off offset:-4096
	global_load_dwordx4 v[46:49], v[12:13], off
	v_add_co_u32_e32 v12, vcc, s8, v10
	v_lshrrev_b32_e32 v110, 2, v0
	s_nop 0
	v_addc_co_u32_e32 v13, vcc, 0, v11, vcc
	v_or_b32_e32 v14, 0x4000, v104
	global_load_dwordx4 v[50:53], v[12:13], off
	global_load_dwordx4 v[54:57], v14, s[2:3]
	s_movk_i32 s2, 0x5000
	v_add_co_u32_e32 v10, vcc, s2, v10
	s_movk_i32 s2, 0xc0
	v_or_b32_e32 v18, 64, v110
	v_addc_co_u32_e32 v11, vcc, 0, v11, vcc
	v_mov_b32_e32 v99, v105
	v_mad_u32_u24 v106, v110, s2, v98
	v_mov_b32_e32 v107, v105
	v_mul_u32_u24_e32 v102, 0xc00, v18
	v_mov_b32_e32 v103, v105
	global_load_dwordx4 v[66:69], v[10:11], off
	v_lshlrev_b64 v[10:11], 4, v[106:107]
	v_lshl_add_u64 v[14:15], s[0:1], 0, v[102:103]
	v_lshlrev_b64 v[16:17], 4, v[98:99]
	v_lshl_add_u64 v[12:13], s[0:1], 0, v[10:11]
	v_lshl_add_u64 v[14:15], v[14:15], 0, v[16:17]
	s_mov_b32 s3, 0x30000
	global_load_dwordx4 v[58:61], v[12:13], off
	global_load_dwordx4 v[62:65], v[14:15], off
	v_add_co_u32_e32 v12, vcc, s3, v14
	s_mov_b32 s3, 0x60000
	s_nop 0
	v_addc_co_u32_e32 v13, vcc, 0, v15, vcc
	v_add_co_u32_e32 v14, vcc, s3, v14
	s_movk_i32 s2, 0xc00
	s_nop 0
	v_addc_co_u32_e32 v15, vcc, 0, v15, vcc
	global_load_dwordx4 v[70:73], v[12:13], off
	global_load_dwordx4 v[74:77], v[14:15], off
	v_mov_b32_e32 v12, 0x90000
	v_mad_u32_u24 v12, v18, s2, v12
	v_mov_b32_e32 v13, v105
	v_mov_b32_e32 v14, 0xc0000
	v_lshl_add_u64 v[12:13], s[0:1], 0, v[12:13]
	v_mad_u32_u24 v100, v18, s2, v14
	v_mov_b32_e32 v101, v105
	v_lshl_add_u64 v[12:13], v[12:13], 0, v[16:17]
	v_lshl_add_u64 v[14:15], s[0:1], 0, v[100:101]
	v_lshl_add_u64 v[14:15], v[14:15], 0, v[16:17]
	global_load_dwordx4 v[78:81], v[12:13], off
	global_load_dwordx4 v[82:85], v[14:15], off
	v_mov_b32_e32 v12, 0xf0000
	v_mad_u32_u24 v96, v18, s2, v12
	v_mov_b32_e32 v97, v105
	v_mov_b32_e32 v14, 0x120000
	v_lshl_add_u64 v[12:13], s[0:1], 0, v[96:97]
	v_mad_u32_u24 v94, v18, s2, v14
	v_mov_b32_e32 v95, v105
	v_lshl_add_u64 v[12:13], v[12:13], 0, v[16:17]
	v_lshl_add_u64 v[14:15], s[0:1], 0, v[94:95]
	v_lshl_add_u64 v[14:15], v[14:15], 0, v[16:17]
	global_load_dwordx4 v[86:89], v[12:13], off
	global_load_dwordx4 v[90:93], v[14:15], off
	s_waitcnt vmcnt(15)
	ds_write_b128 v104, v[2:5] offset:57408
	s_waitcnt vmcnt(14)
	ds_write_b128 v104, v[6:9] offset:61504
	v_lshl_add_u64 v[2:3], s[6:7], 0, v[10:11]
	s_waitcnt lgkmcnt(0)
	s_barrier
	global_load_dwordx4 v[34:37], v[2:3], off
	v_lshl_add_u64 v[2:3], s[4:5], 0, v[10:11]
	v_add_u32_e32 v4, 0x3000, v106
	v_mov_b32_e32 v5, v105
	v_lshl_add_u64 v[4:5], v[4:5], 4, s[4:5]
	global_load_dwordx4 v[30:33], v[2:3], off
	global_load_dwordx4 v[26:29], v[4:5], off
	v_add_u32_e32 v2, 0x6000, v106
	v_mov_b32_e32 v3, v105
	v_lshl_add_u64 v[2:3], v[2:3], 4, s[4:5]
	v_add_u32_e32 v4, 0x9000, v106
	v_mov_b32_e32 v5, v105
	v_lshl_add_u64 v[4:5], v[4:5], 4, s[4:5]
	global_load_dwordx4 v[22:25], v[2:3], off
	global_load_dwordx4 v[18:21], v[4:5], off
	v_add_u32_e32 v2, 0xc000, v106
	v_mov_b32_e32 v3, v105
	v_lshl_add_u64 v[2:3], v[2:3], 4, s[4:5]
	v_add_u32_e32 v4, 0xf000, v106
	v_mov_b32_e32 v5, v105
	v_lshl_add_u64 v[4:5], v[4:5], 4, s[4:5]
	global_load_dwordx4 v[14:17], v[2:3], off
	global_load_dwordx4 v[10:13], v[4:5], off
	v_add_u32_e32 v2, 0x12000, v106
	v_mov_b32_e32 v3, v105
	v_lshl_add_u64 v[108:109], v[2:3], 4, s[4:5]
	v_add_u32_e32 v2, 0x15000, v106
	v_lshl_add_u64 v[106:107], v[2:3], 4, s[4:5]
	global_load_dwordx4 v[6:9], v[108:109], off
	global_load_dwordx4 v[2:5], v[106:107], off
	v_bfe_u32 v113, v0, 5, 1
	v_lshrrev_b32_e32 v115, 6, v0
	v_lshlrev_b32_e32 v112, 2, v113
	v_and_b32_e32 v111, 31, v0
	v_or_b32_e32 v116, v112, v115
	v_lshl_or_b32 v120, v116, 5, v111
	v_lshlrev_b32_e32 v108, 4, v120
	ds_read_b32 v140, v108 offset:57420
	ds_read_b32 v141, v108 offset:61516
	ds_read_u16 v158, v108 offset:57408
	ds_read_u16 v159, v108 offset:61504
	v_lshlrev_b32_e32 v142, 9, v116
	v_add_u32_e32 v142, 0x200, v142
	v_add_u32_e32 v143, 0x1000, v142
	v_mov_b32_e32 v152, 0x2000
	s_waitcnt lgkmcnt(0)
	v_cmp_lt_u32_e64 s[28:29], 12, v158
	v_cmp_lt_u32_e64 s[30:31], 12, v159
	v_ffbl_b32_e32 v153, v140
	v_ffbl_b32_e32 v154, v141
	v_cmp_ne_u32_e32 vcc, 0, v140
	v_cmp_ne_u32_e64 s[22:23], 0, v141
	v_lshl_add_u32 v153, v153, 4, v142
	v_lshl_add_u32 v154, v154, 4, v143
	v_cndmask_b32_e32 v144, v152, v153, vcc
	v_cndmask_b32_e64 v160, v152, v154, s[22:23]
	v_add_u32_e32 v153, -1, v140
	v_add_u32_e32 v154, -1, v141
	v_and_b32_e32 v140, v153, v140
	v_and_b32_e32 v141, v154, v141
	v_ffbl_b32_e32 v153, v140
	v_ffbl_b32_e32 v154, v141
	v_cmp_ne_u32_e32 vcc, 0, v140
	v_cmp_ne_u32_e64 s[22:23], 0, v141
	v_lshl_add_u32 v153, v153, 4, v142
	v_lshl_add_u32 v154, v154, 4, v143
	v_cndmask_b32_e32 v145, v152, v153, vcc
	v_cndmask_b32_e64 v161, v152, v154, s[22:23]
	v_add_u32_e32 v153, -1, v140
	v_add_u32_e32 v154, -1, v141
	v_and_b32_e32 v140, v153, v140
	v_and_b32_e32 v141, v154, v141
	v_ffbl_b32_e32 v153, v140
	v_ffbl_b32_e32 v154, v141
	v_cmp_ne_u32_e32 vcc, 0, v140
	v_cmp_ne_u32_e64 s[22:23], 0, v141
	v_lshl_add_u32 v153, v153, 4, v142
	v_lshl_add_u32 v154, v154, 4, v143
	v_cndmask_b32_e32 v146, v152, v153, vcc
	v_cndmask_b32_e64 v162, v152, v154, s[22:23]
	v_add_u32_e32 v153, -1, v140
	v_add_u32_e32 v154, -1, v141
	v_and_b32_e32 v140, v153, v140
	v_and_b32_e32 v141, v154, v141
	v_ffbl_b32_e32 v153, v140
	v_ffbl_b32_e32 v154, v141
	v_cmp_ne_u32_e32 vcc, 0, v140
	v_cmp_ne_u32_e64 s[22:23], 0, v141
	v_lshl_add_u32 v153, v153, 4, v142
	v_lshl_add_u32 v154, v154, 4, v143
	v_cndmask_b32_e32 v147, v152, v153, vcc
	v_cndmask_b32_e64 v163, v152, v154, s[22:23]
	v_add_u32_e32 v153, -1, v140
	v_add_u32_e32 v154, -1, v141
	v_and_b32_e32 v140, v153, v140
	v_and_b32_e32 v141, v154, v141
	v_ffbl_b32_e32 v153, v140
	v_ffbl_b32_e32 v154, v141
	v_cmp_ne_u32_e32 vcc, 0, v140
	v_cmp_ne_u32_e64 s[22:23], 0, v141
	v_lshl_add_u32 v153, v153, 4, v142
	v_lshl_add_u32 v154, v154, 4, v143
	v_cndmask_b32_e32 v148, v152, v153, vcc
	v_cndmask_b32_e64 v164, v152, v154, s[22:23]
	v_add_u32_e32 v153, -1, v140
	v_add_u32_e32 v154, -1, v141
	v_and_b32_e32 v140, v153, v140
	v_and_b32_e32 v141, v154, v141
	v_lshl_or_b32 v144, v145, 16, v144
	v_lshl_or_b32 v145, v147, 16, v146
	v_lshl_or_b32 v146, v158, 16, v148
	v_mov_b32_e32 v147, v140
	v_lshl_or_b32 v160, v161, 16, v160
	v_lshl_or_b32 v161, v163, 16, v162
	v_lshl_or_b32 v162, v159, 16, v164
	v_mov_b32_e32 v163, v141
	v_add_u32_e32 v153, 0x118c0, v108
	ds_write_b128 v153, v[144:147]
	ds_write_b128 v153, v[160:163] offset:4096
	ds_read_b64 v[106:107], v108 offset:57408
	ds_read_u16 v118, v108 offset:57410
	v_and_b32_e32 v114, 63, v0
	v_and_b32_e32 v0, 32, v0
	v_add_u32_e32 v117, 0xe040, v108
	v_mov_b32_e32 v108, -1
	v_mov_b32_e32 v119, v105
	s_branch .LBB2_2

.LBB2_12:
	s_or_b64 exec, exec, s[12:13]
	v_lshlrev_b32_e32 v106, 9, v119
	v_ffbl_b32_e32 v107, v107
	v_ffbl_b32_e32 v108, v108
	v_lshlrev_b32_e32 v116, 25, v119
	v_lshl_or_b32 v107, v107, 4, v106
	v_mov_b32_e32 v109, 0x2000
	v_lshl_or_b32 v108, v108, 20, v116
	v_bfrev_b32_e32 v116, 4
	v_ffbl_b32_e32 v0, v0
	v_cndmask_b32_e64 v107, v107, v109, s[8:9]
	v_cndmask_b32_e64 v108, v108, v116, s[4:5]
	v_lshl_or_b32 v0, v0, 4, v106
	v_cndmask_b32_e32 v0, v0, v109, vcc
	v_or_b32_e32 v106, v108, v107
	v_mov_b32_e32 v108, 0x800000
	v_lshlrev_b32_e32 v107, 16, v117
	v_cndmask_b32_e64 v108, 0, v108, s[6:7]
	s_waitcnt lgkmcnt(2)
	v_lshl_or_b32 v0, v118, 24, v0
	v_or3_b32 v0, v0, v108, v107
	ds_write2_b32 v105, v106, v0 offset0:1 offset1:3
	v_cmp_ne_u32_e32 vcc, 0, v140
	v_cmp_ne_u32_e64 s[22:23], 0, v141
	v_lshlrev_b32_e32 v150, 5, v113
	v_lshl_add_u32 v155, v113, 2, v115
	v_lshlrev_b32_e32 v155, 2, v155
	v_add_u32_e32 v155, 0x11840, v155
	v_lshrrev_b64 v[146:147], v150, vcc
	v_lshrrev_b64 v[156:157], v150, s[22:23]
	v_mov_b32_e32 v151, 0x400
	v_cmp_ne_u32_e32 vcc, 0, v146
	v_cmp_ne_u32_e64 s[22:23], 0, v156
	s_nop 1
	v_cndmask_b32_e32 v146, 0, v151, vcc
	v_cndmask_b32_e64 v156, 0, v151, s[22:23]
	v_lshrrev_b64 v[148:149], v150, s[28:29]
	v_lshrrev_b64 v[152:153], v150, s[30:31]
	v_mov_b32_e32 v154, 0x800
	v_cmp_ne_u32_e32 vcc, 0, v148
	v_cmp_ne_u32_e64 s[22:23], 0, v152
	s_nop 1
	v_cndmask_b32_e32 v148, 0, v154, vcc
	v_cndmask_b32_e64 v152, 0, v154, s[22:23]
	v_or_b32_e32 v146, v146, v148
	v_or_b32_e32 v156, v156, v152
	v_lshl_add_u32 v148, v113, 2, v115
	v_lshl_or_b32 v148, v148, 5, v111
	v_lshlrev_b32_e32 v149, 2, v148
	v_add_u32_e32 v149, 0x11040, v149
	v_lshlrev_b32_e32 v148, 4, v148
	ds_read_b32 v152, v149
	ds_read_b32 v153, v149 offset:1024
	s_waitcnt lgkmcnt(0)
	ds_write_b32 v148, v152 offset:57408
	ds_write_b32 v148, v153 offset:61504
	v_cmp_eq_u32_e32 vcc, 0, v111
	s_and_saveexec_b64 s[22:23], vcc
	ds_or_b32 v155, v146
	ds_or_b32 v155, v156 offset:32
	s_or_b64 exec, exec, s[22:23]
	s_movk_i32 s2, 0x2010
	v_mul_u32_u24_e32 v105, 0x2010, v115
	v_cmp_eq_u32_e32 vcc, 0, v114
	s_waitcnt vmcnt(22)
	ds_write_b128 v104, v[38:41] offset:32832
	s_waitcnt vmcnt(21)
	ds_write_b128 v104, v[42:45] offset:36928
	s_waitcnt vmcnt(20)
	ds_write_b128 v104, v[46:49] offset:41024
	s_waitcnt vmcnt(19)
	ds_write_b128 v104, v[50:53] offset:45120
	s_waitcnt vmcnt(18)
	ds_write_b128 v104, v[54:57] offset:49216
	s_waitcnt vmcnt(17)
	ds_write_b128 v104, v[66:69] offset:53312
	s_and_saveexec_b64 s[0:1], vcc
	v_mov_b32_e32 v38, 0
	v_mov_b32_e32 v39, v38
	v_mov_b32_e32 v40, v38
	v_mov_b32_e32 v41, v38
	ds_write_b128 v105, v[38:41] offset:8192
	s_or_b64 exec, exec, s[0:1]
	v_lshlrev_b32_e32 v40, 3, v113
	v_lshlrev_b32_e32 v67, 4, v110
	v_or_b32_e32 v38, 0x1e0, v111
	v_or_b32_e32 v0, 0x8040, v40
	v_mad_u32_u24 v66, v1, s2, v67
	v_mad_u32_u24 v38, v38, 48, v0
	s_waitcnt vmcnt(16)
	ds_write_b128 v66, v[58:61]
	s_waitcnt vmcnt(15)
	ds_write_b128 v66, v[62:65] offset:1024
	s_waitcnt vmcnt(14)
	ds_write_b128 v66, v[70:73] offset:2048
	s_waitcnt vmcnt(13)
	ds_write_b128 v66, v[74:77] offset:3072
	s_waitcnt vmcnt(12)
	ds_write_b128 v66, v[78:81] offset:4096
	s_waitcnt vmcnt(11)
	ds_write_b128 v66, v[82:85] offset:5120
	s_waitcnt vmcnt(10)
	ds_write_b128 v66, v[86:89] offset:6144
	s_waitcnt vmcnt(9)
	ds_write_b128 v66, v[90:93] offset:7168
	v_lshl_add_u32 v116, v113, 3, v105
	v_or_b32_e32 v106, 0x1e0, v111
	v_lshlrev_b32_e32 v138, 4, v106
	v_add_u32_e32 v139, 0x118c0, v138
	v_mul_u32_u24_e32 v156, 48, v106
	v_add_u32_e32 v156, v0, v156
	v_mov_b32_e32 v157, 0x1187c
	v_add_u32_e32 v137, v116, v138
	v_add_u32_e32 v138, 0x200, v138
	v_lshlrev_b32_e32 v160, 4, v111
	v_lshlrev_b32_e32 v161, 3, v111
	v_add_u32_e32 v161, 0x118c0, v161
	v_mul_u32_u24_e32 v162, 48, v111
	v_add_u32_e32 v162, v0, v162
	v_mov_b32_e32 v163, 0x11840
	v_mul_hi_u32_u24_e32 v159, 0x410, v111
	v_mul_u32_u24_e32 v158, 0x410, v111
	v_mov_b32_e32 v107, 0x82000
	v_mad_u64_u32 v[158:159], s[0:1], s20, v107, v[158:159]
	v_lshlrev_b32_e32 v107, 3, v113
	v_or_b32_e32 v158, v158, v107
	v_lshl_add_u64 v[158:159], s[14:15], 0, v[158:159]
	s_mov_b64 s[0:1], 0x79e30
	s_mov_b32 s2, 0xffff7e00
	s_mov_b32 s3, -1
	v_lshl_add_u64 v[158:159], v[158:159], 0, s[0:1]
	v_lshl_add_u32 v107, v114, 2, v163
	v_add_u32_e32 v107, -8, v107
	s_waitcnt lgkmcnt(0)
	s_barrier
	ds_read_b128 v[38:41], v138 offset:56896
	ds_read_b128 v[42:45], v139
	ds_read2_b64 v[56:59], v156 offset1:2
	ds_read_b32 v60, v107
	v_add_u32_e32 v156, 0xfffffa00, v156
	ds_read2_b64 v[52:55], v156 offset1:2
	v_add_u32_e32 v106, -2, v114
	v_cmp_gt_u32_e32 vcc, 16, v106
	s_waitcnt lgkmcnt(0)
	v_cndmask_b32_e32 v60, 0, v60, vcc
	s_nop 1
	v_readlane_b32 s4, v60, 17
	v_readlane_b32 s21, v60, 16
	v_add_u32_sdwa v92, v105, v56 dst_sel:DWORD dst_unused:UNUSED_PAD src0_sel:DWORD src1_sel:WORD_0
	v_add_u32_sdwa v93, v105, v56 dst_sel:DWORD dst_unused:UNUSED_PAD src0_sel:DWORD src1_sel:WORD_1
	v_add_u32_sdwa v106, v105, v57 dst_sel:DWORD dst_unused:UNUSED_PAD src0_sel:DWORD src1_sel:WORD_0
	v_add_u32_sdwa v107, v105, v57 dst_sel:DWORD dst_unused:UNUSED_PAD src0_sel:DWORD src1_sel:WORD_1
	v_add_u32_sdwa v108, v105, v58 dst_sel:DWORD dst_unused:UNUSED_PAD src0_sel:DWORD src1_sel:WORD_0
	v_add_u32_sdwa v109, v105, v58 dst_sel:DWORD dst_unused:UNUSED_PAD src0_sel:DWORD src1_sel:WORD_1
	ds_read_b128 v[120:123], v92
	ds_read_b128 v[124:127], v93
	ds_read_b128 v[128:131], v106
	ds_read_b128 v[132:135], v107
	ds_read_b128 v[140:143], v108
	ds_read_b128 v[144:147], v109
	v_add_u32_sdwa v88, v116, v42 dst_sel:DWORD dst_unused:UNUSED_PAD src0_sel:DWORD src1_sel:WORD_0
	v_add_u32_sdwa v89, v116, v42 dst_sel:DWORD dst_unused:UNUSED_PAD src0_sel:DWORD src1_sel:WORD_1
	v_add_u32_sdwa v90, v116, v43 dst_sel:DWORD dst_unused:UNUSED_PAD src0_sel:DWORD src1_sel:WORD_0
	v_add_u32_sdwa v91, v116, v43 dst_sel:DWORD dst_unused:UNUSED_PAD src0_sel:DWORD src1_sel:WORD_1
	v_add_u32_sdwa v173, v116, v44 dst_sel:DWORD dst_unused:UNUSED_PAD src0_sel:DWORD src1_sel:WORD_0
	v_bfe_u32 v117, v41, 16, 7
	v_add_u32_sdwa v118, v116, v39 dst_sel:DWORD dst_unused:UNUSED_PAD src0_sel:DWORD src1_sel:WORD_0
	v_add_u32_sdwa v119, v116, v39 dst_sel:DWORD dst_unused:UNUSED_PAD src0_sel:DWORD src1_sel:WORD_1
	v_add_u32_sdwa v136, v116, v41 dst_sel:DWORD dst_unused:UNUSED_PAD src0_sel:DWORD src1_sel:WORD_0
	s_and_b32 s9, s4, 0xff
	s_waitcnt lgkmcnt(0)
	v_pk_add_f32 v[120:121], v[120:121], v[124:125]
	v_pk_add_f32 v[122:123], v[122:123], v[126:127]
	v_pk_add_f32 v[128:129], v[128:129], v[132:133]
	v_pk_add_f32 v[130:131], v[130:131], v[134:135]
	v_pk_add_f32 v[140:141], v[140:141], v[144:145]
	v_pk_add_f32 v[142:143], v[142:143], v[146:147]
	s_and_b32 s24, s4, 0x900
	s_cbranch_scc1 .Lfarx_pre

.Lslowlev_A:
	v_and_b32_e32 v165, 0x800000, v41
	v_mov_b32_e32 v167, v38
	v_lshlrev_b32_e32 v166, 4, v111
	v_sub_u32_e32 v166, v137, v166
	s_waitcnt lgkmcnt(0)
	v_pk_fma_f32 v[80:81], v[40:41], v[82:83], v[78:79] op_sel_hi:[0,1,1]
	s_nop 0
	v_pk_fma_f32 v[80:81], v[40:41], v[84:85], v[80:81] op_sel_hi:[0,1,1]
	s_mov_b64 exec, s[6:7]
	v_pk_fma_f32 v[80:81], v[40:41], v[86:87], v[80:81] op_sel_hi:[0,1,1]
	v_cmp_ne_u32_e32 vcc, 0, v165
	s_and_saveexec_b64 s[12:13], vcc
	s_cbranch_execz .Lxr1_A
.Lxl1_A:
	v_ffbl_b32_e32 v92, v167
	v_lshl_add_u32 v92, v92, 4, v166
	ds_read_b64 v[64:65], v92
	v_add_u32_e32 v93, -1, v167
	v_and_b32_e32 v167, v93, v167
	s_waitcnt lgkmcnt(0)
	v_pk_fma_f32 v[80:81], v[40:41], v[64:65], v[80:81] op_sel_hi:[0,1,1]
	v_cmp_ne_u32_e32 vcc, 0, v167
	s_and_b64 exec, exec, vcc
	s_cbranch_execnz .Lxl1_A
.Lxr1_A:
	s_mov_b64 exec, s[6:7]
	ds_write_b64 v137, v[80:81]
	s_mov_b64 exec, -1
	s_cmp_lt_u32 s9, 2
	s_cbranch_scc1 .Lnp_A
	ds_read_b64 v[82:83], v118
	ds_read_b64 v[84:85], v119
	ds_read_b64 v[86:87], v136
	v_add_u32_sdwa v88, v116, v180 dst_sel:DWORD dst_unused:UNUSED_PAD src0_sel:DWORD src1_sel:WORD_0
	v_add_u32_sdwa v89, v116, v180 dst_sel:DWORD dst_unused:UNUSED_PAD src0_sel:DWORD src1_sel:WORD_1
	v_add_u32_sdwa v90, v116, v181 dst_sel:DWORD dst_unused:UNUSED_PAD src0_sel:DWORD src1_sel:WORD_0
	v_add_u32_sdwa v91, v116, v181 dst_sel:DWORD dst_unused:UNUSED_PAD src0_sel:DWORD src1_sel:WORD_1
	v_add_u32_sdwa v173, v116, v182 dst_sel:DWORD dst_unused:UNUSED_PAD src0_sel:DWORD src1_sel:WORD_0
	v_bfe_u32 v168, v49, 16, 7
	v_add_u32_sdwa v169, v116, v47 dst_sel:DWORD dst_unused:UNUSED_PAD src0_sel:DWORD src1_sel:WORD_0
	v_add_u32_sdwa v170, v116, v47 dst_sel:DWORD dst_unused:UNUSED_PAD src0_sel:DWORD src1_sel:WORD_1
	v_add_u32_sdwa v171, v116, v49 dst_sel:DWORD dst_unused:UNUSED_PAD src0_sel:DWORD src1_sel:WORD_0
	v_add_u32_e32 v156, 0xfffffa00, v156
	v_add_u32_e32 v172, 0xfffffe00, v137
	v_readlane_b32 s4, v60, s5
	v_max_i32_e32 v156, v156, v162
	v_lshl_add_u64 v[158:159], v[158:159], 0, s[2:3]
	s_and_b32 s23, s21, 0xff
	s_waitcnt lgkmcnt(0)
	v_pk_fma_f32 v[80:81], v[40:41], v[82:83], v[78:79] op_sel_hi:[0,1,1]
	s_nop 0
	v_pk_fma_f32 v[80:81], v[40:41], v[84:85], v[80:81] op_sel_hi:[0,1,1]
	s_mov_b64 exec, s[26:27]
	v_pk_fma_f32 v[80:81], v[40:41], v[86:87], v[80:81] op_sel_hi:[0,1,1]
	v_cmp_ne_u32_e32 vcc, 0, v165
	s_and_saveexec_b64 s[12:13], vcc
	s_cbranch_execz .Lxr2_A

.Lxr2_A:
	s_mov_b64 exec, s[26:27]
	ds_write_b64 v137, v[80:81]
	s_mov_b64 exec, -1
	s_cmp_lt_u32 s9, 3
	s_cbranch_scc1 .Lbot_A
	s_mov_b32 s8, 3
.Lxlev_A:
	ds_read_b64 v[82:83], v118
	ds_read_b64 v[84:85], v119
	ds_read_b64 v[86:87], v136
	v_cmp_eq_u32_e64 s[6:7], s8, v117
	s_add_u32 s8, s8, 1
	s_mov_b64 exec, s[6:7]
	s_waitcnt lgkmcnt(2)
	v_pk_fma_f32 v[80:81], v[40:41], v[82:83], v[78:79] op_sel_hi:[0,1,1]
	s_waitcnt lgkmcnt(1)
	v_pk_fma_f32 v[80:81], v[40:41], v[84:85], v[80:81] op_sel_hi:[0,1,1]
	s_waitcnt lgkmcnt(0)
	v_pk_fma_f32 v[80:81], v[40:41], v[86:87], v[80:81] op_sel_hi:[0,1,1]
	v_cmp_ne_u32_e32 vcc, 0, v165
	s_and_saveexec_b64 s[12:13], vcc
	s_cbranch_execz .Lxr3_A

.Lxr3_A:
	s_mov_b64 exec, s[6:7]
	ds_write_b64 v137, v[80:81]
	s_mov_b64 exec, -1
	s_cmp_le_u32 s8, s9
	s_cbranch_scc1 .Lxlev_A
	s_branch .Lbot_A
.Lnp_B:
	s_waitcnt lgkmcnt(0)
	v_add_u32_sdwa v88, v116, v42 dst_sel:DWORD dst_unused:UNUSED_PAD src0_sel:DWORD src1_sel:WORD_0
	v_add_u32_sdwa v89, v116, v42 dst_sel:DWORD dst_unused:UNUSED_PAD src0_sel:DWORD src1_sel:WORD_1
	v_add_u32_sdwa v90, v116, v43 dst_sel:DWORD dst_unused:UNUSED_PAD src0_sel:DWORD src1_sel:WORD_0
	v_add_u32_sdwa v91, v116, v43 dst_sel:DWORD dst_unused:UNUSED_PAD src0_sel:DWORD src1_sel:WORD_1
	v_add_u32_sdwa v173, v116, v44 dst_sel:DWORD dst_unused:UNUSED_PAD src0_sel:DWORD src1_sel:WORD_0
	v_bfe_u32 v117, v41, 16, 7
	v_add_u32_sdwa v118, v116, v39 dst_sel:DWORD dst_unused:UNUSED_PAD src0_sel:DWORD src1_sel:WORD_0
	v_add_u32_sdwa v119, v116, v39 dst_sel:DWORD dst_unused:UNUSED_PAD src0_sel:DWORD src1_sel:WORD_1
	v_add_u32_sdwa v136, v116, v41 dst_sel:DWORD dst_unused:UNUSED_PAD src0_sel:DWORD src1_sel:WORD_0
	v_add_u32_e32 v156, 0xfffffa00, v156
	v_add_u32_e32 v137, 0xfffffe00, v172
	v_readlane_b32 s21, v60, s5
	v_max_i32_e32 v156, v156, v162
	v_lshl_add_u64 v[158:159], v[158:159], 0, s[2:3]
	s_and_b32 s9, s4, 0xff
	s_branch .Lbot_B
.Lslowlev_B:
	v_and_b32_e32 v165, 0x800000, v49
	v_mov_b32_e32 v167, v46
	v_lshlrev_b32_e32 v166, 4, v111
	v_sub_u32_e32 v166, v172, v166
	s_waitcnt lgkmcnt(0)
	v_pk_fma_f32 v[80:81], v[48:49], v[82:83], v[78:79] op_sel_hi:[0,1,1]
	s_nop 0
	v_pk_fma_f32 v[80:81], v[48:49], v[84:85], v[80:81] op_sel_hi:[0,1,1]
	s_mov_b64 exec, s[6:7]
	v_pk_fma_f32 v[80:81], v[48:49], v[86:87], v[80:81] op_sel_hi:[0,1,1]
	v_cmp_ne_u32_e32 vcc, 0, v165
	s_and_saveexec_b64 s[12:13], vcc
	s_cbranch_execz .Lxr1_B
.Lxl1_B:
	v_ffbl_b32_e32 v92, v167
	v_lshl_add_u32 v92, v92, 4, v166
	ds_read_b64 v[64:65], v92
	v_add_u32_e32 v93, -1, v167
	v_and_b32_e32 v167, v93, v167
	s_waitcnt lgkmcnt(0)
	v_pk_fma_f32 v[80:81], v[48:49], v[64:65], v[80:81] op_sel_hi:[0,1,1]
	v_cmp_ne_u32_e32 vcc, 0, v167
	s_and_b64 exec, exec, vcc
	s_cbranch_execnz .Lxl1_B
.Lxr1_B:
	s_mov_b64 exec, s[6:7]
	ds_write_b64 v172, v[80:81]
	s_mov_b64 exec, -1
	s_cmp_lt_u32 s23, 2
	s_cbranch_scc1 .Lnp_B
	ds_read_b64 v[82:83], v169
	ds_read_b64 v[84:85], v170
	ds_read_b64 v[86:87], v171
	v_add_u32_sdwa v88, v116, v42 dst_sel:DWORD dst_unused:UNUSED_PAD src0_sel:DWORD src1_sel:WORD_0
	v_add_u32_sdwa v89, v116, v42 dst_sel:DWORD dst_unused:UNUSED_PAD src0_sel:DWORD src1_sel:WORD_1
	v_add_u32_sdwa v90, v116, v43 dst_sel:DWORD dst_unused:UNUSED_PAD src0_sel:DWORD src1_sel:WORD_0
	v_add_u32_sdwa v91, v116, v43 dst_sel:DWORD dst_unused:UNUSED_PAD src0_sel:DWORD src1_sel:WORD_1
	v_add_u32_sdwa v173, v116, v44 dst_sel:DWORD dst_unused:UNUSED_PAD src0_sel:DWORD src1_sel:WORD_0
	v_bfe_u32 v117, v41, 16, 7
	v_add_u32_sdwa v118, v116, v39 dst_sel:DWORD dst_unused:UNUSED_PAD src0_sel:DWORD src1_sel:WORD_0
	v_add_u32_sdwa v119, v116, v39 dst_sel:DWORD dst_unused:UNUSED_PAD src0_sel:DWORD src1_sel:WORD_1
	v_add_u32_sdwa v136, v116, v41 dst_sel:DWORD dst_unused:UNUSED_PAD src0_sel:DWORD src1_sel:WORD_0
	v_add_u32_e32 v156, 0xfffffa00, v156
	v_add_u32_e32 v137, 0xfffffe00, v172
	v_readlane_b32 s21, v60, s5
	v_max_i32_e32 v156, v156, v162
	v_lshl_add_u64 v[158:159], v[158:159], 0, s[2:3]
	s_and_b32 s9, s4, 0xff
	s_waitcnt lgkmcnt(0)
	v_pk_fma_f32 v[80:81], v[48:49], v[82:83], v[78:79] op_sel_hi:[0,1,1]
	s_nop 0
	v_pk_fma_f32 v[80:81], v[48:49], v[84:85], v[80:81] op_sel_hi:[0,1,1]
	s_mov_b64 exec, s[26:27]
	v_pk_fma_f32 v[80:81], v[48:49], v[86:87], v[80:81] op_sel_hi:[0,1,1]
	v_cmp_ne_u32_e32 vcc, 0, v165
	s_and_saveexec_b64 s[12:13], vcc
	s_cbranch_execz .Lxr2_B

.Lxr2_B:
	s_mov_b64 exec, s[26:27]
	ds_write_b64 v172, v[80:81]
	s_mov_b64 exec, -1
	s_cmp_lt_u32 s23, 3
	s_cbranch_scc1 .Lbot_B
	s_mov_b32 s8, 3
.Lxlev_B:
	ds_read_b64 v[82:83], v169
	ds_read_b64 v[84:85], v170
	ds_read_b64 v[86:87], v171
	v_cmp_eq_u32_e64 s[6:7], s8, v168
	s_add_u32 s8, s8, 1
	s_mov_b64 exec, s[6:7]
	s_waitcnt lgkmcnt(2)
	v_pk_fma_f32 v[80:81], v[48:49], v[82:83], v[78:79] op_sel_hi:[0,1,1]
	s_waitcnt lgkmcnt(1)
	v_pk_fma_f32 v[80:81], v[48:49], v[84:85], v[80:81] op_sel_hi:[0,1,1]
	s_waitcnt lgkmcnt(0)
	v_pk_fma_f32 v[80:81], v[48:49], v[86:87], v[80:81] op_sel_hi:[0,1,1]
	v_cmp_ne_u32_e32 vcc, 0, v165
	s_and_saveexec_b64 s[12:13], vcc
	s_cbranch_execz .Lxr3_B

.Lxr3_B:
	s_mov_b64 exec, s[6:7]
	ds_write_b64 v172, v[80:81]
	s_mov_b64 exec, -1
	s_cmp_le_u32 s8, s23
	s_cbranch_scc1 .Lxlev_B
	s_branch .Lbot_B
.Lfarx_pre:
	s_waitcnt lgkmcnt(0)
	v_add_u32_sdwa v92, v105, v59 dst_sel:DWORD dst_unused:UNUSED_PAD src0_sel:DWORD src1_sel:WORD_0
	v_add_u32_sdwa v93, v105, v59 dst_sel:DWORD dst_unused:UNUSED_PAD src0_sel:DWORD src1_sel:WORD_1
	ds_read_b128 v[148:151], v92
	ds_read_b128 v[152:155], v93
	s_waitcnt lgkmcnt(0)
	v_pk_add_f32 v[148:149], v[148:149], v[152:153]
	v_pk_add_f32 v[150:151], v[150:151], v[154:155]
	v_pk_add_f32 v[140:141], v[140:141], v[148:149]
	v_pk_add_f32 v[142:143], v[142:143], v[150:151]
	s_bitcmp1_b32 s4, 8
	s_cbranch_scc0 .Lfarslow_ret_pre
	s_branch .Lfarslow_pre

.Lfarslow_pre:
	s_waitcnt lgkmcnt(0)
	v_sub_u32_e32 v165, v137, v116
	v_mul_u32_u24_e32 v165, 3, v165
	v_add_u32_e32 v165, v0, v165
	v_add_u32_e32 v165, 32, v165
	ds_read_b64 v[64:65], v165
	v_lshrrev_b32_e32 v164, 16, v44
	v_mov_b64_e32 v[166:167], v[158:159]
	s_movk_i32 s22, 24
	s_waitcnt lgkmcnt(0)

.Lfarslow_A:
	s_waitcnt lgkmcnt(0)
	v_sub_u32_e32 v165, v137, v116
	v_mul_u32_u24_e32 v165, 3, v165
	v_add_u32_e32 v165, v0, v165
	v_add_u32_e32 v165, -1504, v165
	ds_read_b64 v[64:65], v165
	v_lshrrev_b32_e32 v164, 16, v182
	v_mov_b64_e32 v[166:167], v[158:159]
	s_movk_i32 s22, 24
	s_waitcnt lgkmcnt(0)

.Lfarslow_B:
	s_waitcnt lgkmcnt(0)
	v_sub_u32_e32 v165, v172, v116
	v_mul_u32_u24_e32 v165, 3, v165
	v_add_u32_e32 v165, v0, v165
	v_add_u32_e32 v165, -1504, v165
	ds_read_b64 v[64:65], v165
	v_lshrrev_b32_e32 v164, 16, v44
	v_mov_b64_e32 v[166:167], v[158:159]
	s_movk_i32 s22, 24
	s_waitcnt lgkmcnt(0)

.Lnearslow_end_B:
	s_mov_b64 exec, -1
	s_branch .Lnearslow_ret_B
.Lchain_done:
.LBB2_44:
	v_mov_b32_e32 v0, 0x10040
	v_lshl_or_b32 v54, v1, 4, v0
	v_lshl_add_u32 v0, v110, 6, v54
	v_add_u32_e32 v55, 0x4c, v67
	s_waitcnt vmcnt(8)
	ds_write_b128 v0, v[34:37]
	s_waitcnt lgkmcnt(0)
	s_barrier
	ds_read2st64_b32 v[0:1], v55 offset0:224 offset1:228
	s_add_u32 s0, s16, s18
	s_addc_u32 s1, s17, s19
	v_lshl_add_u64 v[50:51], v[98:99], 4, s[0:1]
	v_mul_u32_u24_e32 v38, 0xc00, v110
	s_waitcnt lgkmcnt(0)
	v_lshrrev_b32_e32 v0, 24, v0
	v_lshl_add_u32 v0, v0, 6, v54
	v_mov_b32_e32 v39, 0
	ds_read_b128 v[34:37], v66
	v_lshl_add_u64 v[52:53], v[50:51], 0, v[38:39]
	ds_read_b128 v[38:41], v0
	ds_read_b128 v[42:45], v66 offset:1024
	v_lshrrev_b32_e32 v0, 24, v1
	v_lshl_add_u32 v0, v0, 6, v54
	ds_read_b128 v[46:49], v0
	s_waitcnt vmcnt(7) lgkmcnt(3)
	v_pk_add_f32 v[30:31], v[34:35], v[30:31]
	v_pk_add_f32 v[0:1], v[36:37], v[32:33]
	s_waitcnt vmcnt(6) lgkmcnt(1)
	v_pk_add_f32 v[26:27], v[42:43], v[26:27]
	v_pk_add_f32 v[28:29], v[44:45], v[28:29]
	v_pk_add_f32 v[30:31], v[30:31], v[38:39]
	v_pk_add_f32 v[32:33], v[0:1], v[40:41]
	v_lshl_add_u64 v[0:1], v[50:51], 0, v[102:103]
	s_waitcnt lgkmcnt(0)
	v_pk_add_f32 v[26:27], v[26:27], v[46:47]
	ds_read2st64_b32 v[38:39], v55 offset0:232 offset1:236
	v_pk_add_f32 v[28:29], v[28:29], v[48:49]
	global_store_dwordx4 v[52:53], v[30:33], off
	global_store_dwordx4 v[0:1], v[26:29], off
	ds_read_b128 v[26:29], v66 offset:2048
	s_waitcnt lgkmcnt(1)
	v_lshrrev_b32_e32 v30, 24, v38
	v_lshl_add_u32 v30, v30, 6, v54
	ds_read_b128 v[30:33], v30
	ds_read_b128 v[34:37], v66 offset:3072
	s_mov_b32 s0, 0x30000
	s_waitcnt vmcnt(7) lgkmcnt(2)
	v_pk_add_f32 v[22:23], v[26:27], v[22:23]
	v_lshrrev_b32_e32 v26, 24, v39
	v_lshl_add_u32 v26, v26, 6, v54
	ds_read_b128 v[38:41], v26
	v_add_co_u32_e32 v26, vcc, s0, v0
	s_mov_b32 s0, 0x60000
	s_nop 0
	v_addc_co_u32_e32 v27, vcc, 0, v1, vcc
	s_waitcnt lgkmcnt(2)
	v_pk_add_f32 v[22:23], v[22:23], v[30:31]
	s_waitcnt vmcnt(6) lgkmcnt(1)
	v_pk_add_f32 v[18:19], v[34:35], v[18:19]
	v_pk_add_f32 v[20:21], v[36:37], v[20:21]
	ds_read2st64_b32 v[30:31], v55 offset0:240 offset1:244
	v_add_co_u32_e32 v0, vcc, s0, v0
	s_waitcnt lgkmcnt(1)
	v_pk_add_f32 v[18:19], v[18:19], v[38:39]
	v_pk_add_f32 v[20:21], v[20:21], v[40:41]
	v_addc_co_u32_e32 v1, vcc, 0, v1, vcc
	global_store_dwordx4 v[0:1], v[18:21], off
	ds_read_b128 v[18:21], v66 offset:4096
	v_pk_add_f32 v[24:25], v[28:29], v[24:25]
	s_waitcnt lgkmcnt(1)
	v_lshrrev_b32_e32 v0, 24, v30
	v_pk_add_f32 v[24:25], v[24:25], v[32:33]
	global_store_dwordx4 v[26:27], v[22:25], off
	v_lshl_add_u32 v0, v0, 6, v54
	ds_read_b128 v[22:25], v0
	ds_read_b128 v[26:29], v66 offset:5120
	s_waitcnt vmcnt(7) lgkmcnt(2)
	v_pk_add_f32 v[0:1], v[18:19], v[14:15]
	v_lshrrev_b32_e32 v14, 24, v31
	v_lshl_add_u32 v14, v14, 6, v54
	ds_read_b128 v[30:33], v14
	s_waitcnt lgkmcnt(2)
	v_pk_add_f32 v[14:15], v[0:1], v[22:23]
	v_pk_add_f32 v[0:1], v[20:21], v[16:17]
	s_mov_b32 s0, 0xc0000
	v_pk_add_f32 v[16:17], v[0:1], v[24:25]
	v_add_co_u32_e32 v0, vcc, s0, v52
	s_waitcnt vmcnt(6) lgkmcnt(1)
	v_pk_add_f32 v[10:11], v[26:27], v[10:11]
	v_addc_co_u32_e32 v1, vcc, 0, v53, vcc
	v_pk_add_f32 v[12:13], v[28:29], v[12:13]
	global_store_dwordx4 v[0:1], v[14:17], off
	v_lshl_add_u64 v[0:1], v[50:51], 0, v[100:101]
	ds_read2st64_b32 v[22:23], v55 offset0:248 offset1:252
	s_waitcnt lgkmcnt(1)
	v_pk_add_f32 v[10:11], v[10:11], v[30:31]
	v_pk_add_f32 v[12:13], v[12:13], v[32:33]
	global_store_dwordx4 v[0:1], v[10:13], off
	ds_read_b128 v[10:13], v66 offset:6144
	s_waitcnt lgkmcnt(1)
	v_lshrrev_b32_e32 v0, 24, v22
	v_lshl_add_u32 v14, v0, 6, v54
	ds_read_b128 v[14:17], v14
	ds_read_b128 v[18:21], v66 offset:7168
	v_lshl_add_u64 v[0:1], v[50:51], 0, v[96:97]
	s_waitcnt vmcnt(7) lgkmcnt(2)
	v_pk_add_f32 v[6:7], v[10:11], v[6:7]
	v_lshrrev_b32_e32 v10, 24, v23
	v_lshl_add_u32 v10, v10, 6, v54
	ds_read_b128 v[22:25], v10
	v_pk_add_f32 v[8:9], v[12:13], v[8:9]
	s_waitcnt lgkmcnt(2)
	v_pk_add_f32 v[6:7], v[6:7], v[14:15]
	v_pk_add_f32 v[8:9], v[8:9], v[16:17]
	global_store_dwordx4 v[0:1], v[6:9], off
	s_waitcnt vmcnt(7) lgkmcnt(1)
	v_pk_add_f32 v[0:1], v[18:19], v[2:3]
	v_pk_add_f32 v[2:3], v[20:21], v[4:5]
	v_lshl_add_u64 v[6:7], v[50:51], 0, v[94:95]
	s_waitcnt lgkmcnt(0)
	v_pk_add_f32 v[0:1], v[0:1], v[22:23]
	v_pk_add_f32 v[2:3], v[2:3], v[24:25]
	global_store_dwordx4 v[6:7], v[0:3], off
	s_endpgm
